# static s_setprio 1 for waves 4-7 during the 19 GEMM phases (reset at each phase end)
# baseline (speedup 1.0000x reference)
.LBB0_348:
	s_cmp_gt_i32 s6, 2
	s_cselect_b64 s[0:1], -1, 0
	s_cmp_lt_i32 s7, 3
	s_cselect_b64 s[2:3], -1, 0
	s_or_b64 s[0:1], s[0:1], s[2:3]
	s_and_b64 vcc, exec, s[0:1]
	s_cbranch_vccnz .LBB0_428
	s_mov_b32 s98, s88
	s_and_b32 s99, s88, 31
	s_lshl_b32 s99, s99, 3
	s_lshr_b32 s88, s88, 5
	s_or_b32 s88, s88, s99
	v_readlane_b32 s99, v253, 20
	s_nop 3
	s_cmp_lt_u32 s99, 4
	s_cbranch_scc1 .Lgprio_0
	s_setprio 1
.Lgprio_0:
	s_add_u32 s11, s94, 0x3d600000
	s_addc_u32 s30, s95, 0
	s_lshl_b32 s0, s88, 3
	v_readlane_b32 s1, v253, 20
	s_add_i32 s0, s0, s1
	s_cmpk_gt_i32 s0, 0xfff
	s_waitcnt vmcnt(3)
	v_mbcnt_lo_u32_b32 v0, -1, 0
	v_mbcnt_hi_u32_b32 v0, -1, v0
	s_cbranch_scc1 .LBB0_354
	v_readlane_b32 s3, v253, 20
	s_lshl_b32 s1, s88, 4
	s_lshl_b32 s3, s3, 1
	s_add_i32 s8, s1, s3
	s_ashr_i32 s1, s0, 31
	s_lshl_b32 s2, s90, 3
	s_lshl_b32 s9, s90, 4
	s_lshl_b64 s[4:5], s[0:1], 12
	v_lshlrev_b32_e32 v2, 6, v0
	s_add_u32 s4, s94, s4
	v_ashrrev_i32_e32 v3, 31, v2
	s_addc_u32 s5, s95, s5
	v_cmp_eq_u32_e32 vcc, 0, v0
	v_lshl_add_u64 v[0:1], s[4:5], 0, v[2:3]
	s_mov_b64 s[4:5], 0x37600000
	s_ashr_i32 s3, s2, 31
	v_lshl_add_u64 v[0:1], v[0:1], 0, s[4:5]
	s_lshl_b64 s[4:5], s[2:3], 12
	v_mov_b32_e32 v2, 0
	s_movk_i32 s1, 0x7fff
	v_mov_b32_e32 v3, 0x800000
	s_branch .LBB0_352

.LBB0_378:
	v_readlane_b32 s6, v253, 23
	v_readlane_b32 s7, v253, 24
	s_mov_b32 s88, s98
	s_setprio 0
	s_cmp_gt_u32 s7, 3
	s_cbranch_scc0 .LBB0_428
	v_readlane_b32 s0, v253, 20
	s_waitcnt vmcnt(0)
	s_lshl_b32 s0, s0, 6
	s_sub_i32 s0, 0, s0
	s_waitcnt vmcnt(0)
	s_barrier
	v_mbcnt_lo_u32_b32 v0, -1, 0
	v_mbcnt_hi_u32_b32 v0, -1, v0
	s_nop 0
	v_cmp_eq_u32_e32 vcc, s0, v0
	s_and_saveexec_b64 s[0:1], vcc
	s_cbranch_execz .LBB0_427
	s_add_i32 s2, 0, 0x20160
	v_mov_b32_e32 v0, s2
	s_waitcnt vmcnt(0) expcnt(0) lgkmcnt(0)
	ds_read_b32 v2, v0
	s_add_i32 s2, 0, 0x20164
	v_mov_b32_e32 v0, s2
	ds_read_b32 v0, v0
	s_waitcnt lgkmcnt(1)
	v_cmp_ne_u32_e32 vcc, 0, v2
	s_cbranch_vccnz .LBB0_395
	v_readlane_b32 s2, v253, 0
	v_readlane_b32 s3, v253, 1
	s_load_dwordx2 s[6:7], s[2:3], 0x4
	s_add_u32 s2, s94, 0x4200
	s_addc_u32 s3, s95, 0
	s_add_u32 s4, s94, 0x4400
	s_addc_u32 s5, s95, 0
	s_waitcnt lgkmcnt(0)
	s_mul_i32 s33, s6, s90
	s_add_u32 s6, s94, 0x4500
	s_mul_i32 s33, s33, s7
	s_addc_u32 s7, s95, 0
	s_add_u32 s8, s94, 0x4600
	s_addc_u32 s9, s95, 0
	s_add_u32 s10, s94, 0x4700
	s_addc_u32 s11, s95, 0
	s_add_u32 s12, s94, 0x4800
	s_addc_u32 s13, s95, 0
	s_add_u32 s14, s94, 0x4900
	s_addc_u32 s15, s95, 0
	s_add_u32 s16, s94, 0x4a00
	s_addc_u32 s17, s95, 0
	s_add_u32 s18, s94, 0x4b00
	s_addc_u32 s19, s95, 0
	s_add_u32 s20, s94, 0x4c00
	s_addc_u32 s21, s95, 0
	s_add_u32 s22, s94, 0x4d00
	s_addc_u32 s23, s95, 0
	s_add_u32 s24, s94, 0x4e00
	s_addc_u32 s25, s95, 0
	s_add_u32 s26, s94, 0x4f00
	s_addc_u32 s27, s95, 0
	s_add_u32 s28, s94, 0x5000
	s_addc_u32 s29, s95, 0
	s_add_u32 s30, s94, 0x5100
	s_addc_u32 s31, s95, 0
	s_add_u32 s34, s94, 0x5200
	s_addc_u32 s35, s95, 0
	s_add_u32 s36, s94, 0x5300
	s_addc_u32 s37, s95, 0
	s_mov_b32 s44, 1
	v_mov_b32_e32 v16, 0
	s_branch .LBB0_383

.LBB0_428:
	s_cmp_gt_i32 s6, 3
	s_cselect_b64 s[0:1], -1, 0
	s_cmp_lt_i32 s7, 4
	s_cselect_b64 s[2:3], -1, 0
	s_or_b64 s[0:1], s[0:1], s[2:3]
	s_and_b64 vcc, exec, s[0:1]
	s_cbranch_vccnz .LBB0_545
	s_mov_b32 s98, s88
	s_and_b32 s99, s88, 31
	s_lshl_b32 s99, s99, 3
	s_lshr_b32 s88, s88, 5
	s_or_b32 s88, s88, s99
	v_readlane_b32 s99, v253, 20
	s_nop 3
	s_cmp_lt_u32 s99, 4
	s_cbranch_scc1 .Lgprio_1
	s_setprio 1
.Lgprio_1:
	s_cmpk_lt_i32 s88, 0x84
	s_cselect_b64 s[2:3], -1, 0
	s_cmpk_gt_i32 s88, 0x83
	s_waitcnt vmcnt(0)
	v_mbcnt_lo_u32_b32 v0, -1, 0
	v_mbcnt_hi_u32_b32 v0, -1, v0
	v_mbcnt_lo_u32_b32 v4, -1, 0
	v_mbcnt_hi_u32_b32 v4, -1, v4
	s_cbranch_scc1 .LBB0_432
	s_ashr_i32 s0, s88, 31
	s_lshr_b32 s0, s0, 29
	s_add_i32 s4, s88, s0
	s_and_b32 s0, s4, -8
	s_sub_i32 s5, s88, s0
	s_cmp_gt_i32 s5, 3
	s_cbranch_scc0 .LBB0_433
	s_lshl_b32 s0, s5, 4
	s_or_b32 s6, s0, 4
	s_cbranch_execz .LBB0_434
	s_branch .LBB0_435

.LBB0_495:
	v_readlane_b32 s6, v253, 23
	v_readlane_b32 s7, v253, 24
	s_mov_b32 s88, s98
	s_setprio 0
	s_cmp_lt_u32 s7, 5
	s_cbranch_scc1 .LBB0_545
	v_readlane_b32 s0, v253, 20
	s_waitcnt vmcnt(0)
	s_lshl_b32 s0, s0, 6
	s_sub_i32 s0, 0, s0
	s_waitcnt vmcnt(0)
	s_barrier
	v_mbcnt_lo_u32_b32 v0, -1, 0
	v_mbcnt_hi_u32_b32 v0, -1, v0
	s_nop 0
	v_cmp_eq_u32_e32 vcc, s0, v0
	s_and_saveexec_b64 s[0:1], vcc
	s_cbranch_execz .LBB0_544
	s_add_i32 s2, 0, 0x20160
	v_mov_b32_e32 v0, s2
	s_waitcnt vmcnt(0) expcnt(0) lgkmcnt(0)
	ds_read_b32 v2, v0
	s_add_i32 s2, 0, 0x20164
	v_mov_b32_e32 v0, s2
	ds_read_b32 v0, v0
	s_waitcnt lgkmcnt(1)
	v_cmp_ne_u32_e32 vcc, 0, v2
	s_cbranch_vccnz .LBB0_512
	v_readlane_b32 s2, v253, 0
	v_readlane_b32 s3, v253, 1
	s_load_dwordx2 s[6:7], s[2:3], 0x4
	s_add_u32 s2, s94, 0x4200
	s_addc_u32 s3, s95, 0
	s_add_u32 s4, s94, 0x4400
	s_addc_u32 s5, s95, 0
	s_waitcnt lgkmcnt(0)
	s_mul_i32 s33, s6, s90
	s_add_u32 s6, s94, 0x4500
	s_mul_i32 s33, s33, s7
	s_addc_u32 s7, s95, 0
	s_add_u32 s8, s94, 0x4600
	s_addc_u32 s9, s95, 0
	s_add_u32 s10, s94, 0x4700
	s_addc_u32 s11, s95, 0
	s_add_u32 s12, s94, 0x4800
	s_addc_u32 s13, s95, 0
	s_add_u32 s14, s94, 0x4900
	s_addc_u32 s15, s95, 0
	s_add_u32 s16, s94, 0x4a00
	s_addc_u32 s17, s95, 0
	s_add_u32 s18, s94, 0x4b00
	s_addc_u32 s19, s95, 0
	s_add_u32 s20, s94, 0x4c00
	s_addc_u32 s21, s95, 0
	s_add_u32 s22, s94, 0x4d00
	s_addc_u32 s23, s95, 0
	s_add_u32 s24, s94, 0x4e00
	s_addc_u32 s25, s95, 0
	s_add_u32 s26, s94, 0x4f00
	s_addc_u32 s27, s95, 0
	s_add_u32 s28, s94, 0x5000
	s_addc_u32 s29, s95, 0
	s_add_u32 s30, s94, 0x5100
	s_addc_u32 s31, s95, 0
	s_add_u32 s34, s94, 0x5200
	s_addc_u32 s35, s95, 0
	s_add_u32 s36, s94, 0x5300
	s_addc_u32 s37, s95, 0
	s_mov_b32 s44, 1
	v_mov_b32_e32 v16, 0
	s_branch .LBB0_500

.LBB0_545:
	s_cmp_gt_i32 s6, 4
	s_cselect_b64 s[0:1], -1, 0
	s_cmp_lt_i32 s7, 5
	s_cselect_b64 s[2:3], -1, 0
	s_or_b64 s[0:1], s[0:1], s[2:3]
	s_and_b64 vcc, exec, s[0:1]
	s_cbranch_vccnz .LBB0_622
	s_mov_b32 s98, s88
	s_and_b32 s99, s88, 31
	s_lshl_b32 s99, s99, 3
	s_lshr_b32 s88, s88, 5
	s_or_b32 s88, s88, s99
	v_readlane_b32 s99, v253, 20
	s_nop 3
	s_cmp_lt_u32 s99, 4
	s_cbranch_scc1 .Lgprio_2
	s_setprio 1
.Lgprio_2:
	s_cmpk_gt_i32 s88, 0xff
	s_waitcnt vmcnt(0)
	v_mbcnt_lo_u32_b32 v0, -1, 0
	v_mbcnt_hi_u32_b32 v0, -1, v0
	v_mbcnt_lo_u32_b32 v9, -1, 0
	v_mbcnt_hi_u32_b32 v9, -1, v9
	s_cbranch_scc1 .LBB0_572
	s_ashr_i32 s28, s88, 31
	s_lshr_b32 s0, s28, 29
	s_add_i32 s3, s88, s0
	s_and_b32 s0, s3, -8
	s_sub_i32 s4, s88, s0
	s_cmp_gt_i32 s4, -1
	s_cbranch_scc0 .LBB0_549
	s_lshl_b32 s2, s4, 5
	s_cbranch_execz .LBB0_550
	s_branch .LBB0_551

.LBB0_572:
	v_readlane_b32 s6, v253, 23
	v_readlane_b32 s7, v253, 24
	s_mov_b32 s88, s98
	s_setprio 0
	s_cmp_lt_u32 s7, 6
	s_cbranch_scc1 .LBB0_622
	v_readlane_b32 s0, v253, 20
	s_waitcnt vmcnt(0)
	s_lshl_b32 s0, s0, 6
	s_sub_i32 s0, 0, s0
	s_waitcnt vmcnt(0)
	s_barrier
	v_mbcnt_lo_u32_b32 v0, -1, 0
	v_mbcnt_hi_u32_b32 v0, -1, v0
	s_nop 0
	v_cmp_eq_u32_e32 vcc, s0, v0
	s_and_saveexec_b64 s[0:1], vcc
	s_cbranch_execz .LBB0_621
	s_add_i32 s2, 0, 0x20160
	v_mov_b32_e32 v0, s2
	s_waitcnt vmcnt(0) expcnt(0) lgkmcnt(0)
	ds_read_b32 v2, v0
	s_add_i32 s2, 0, 0x20164
	v_mov_b32_e32 v0, s2
	ds_read_b32 v0, v0
	s_waitcnt lgkmcnt(1)
	v_cmp_ne_u32_e32 vcc, 0, v2
	s_cbranch_vccnz .LBB0_589
	v_readlane_b32 s2, v253, 0
	v_readlane_b32 s3, v253, 1
	s_load_dwordx2 s[6:7], s[2:3], 0x4
	s_add_u32 s2, s94, 0x4200
	s_addc_u32 s3, s95, 0
	s_add_u32 s4, s94, 0x4400
	s_addc_u32 s5, s95, 0
	s_waitcnt lgkmcnt(0)
	s_mul_i32 s33, s6, s90
	s_add_u32 s6, s94, 0x4500
	s_mul_i32 s33, s33, s7
	s_addc_u32 s7, s95, 0
	s_add_u32 s8, s94, 0x4600
	s_addc_u32 s9, s95, 0
	s_add_u32 s10, s94, 0x4700
	s_addc_u32 s11, s95, 0
	s_add_u32 s12, s94, 0x4800
	s_addc_u32 s13, s95, 0
	s_add_u32 s14, s94, 0x4900
	s_addc_u32 s15, s95, 0
	s_add_u32 s16, s94, 0x4a00
	s_addc_u32 s17, s95, 0
	s_add_u32 s18, s94, 0x4b00
	s_addc_u32 s19, s95, 0
	s_add_u32 s20, s94, 0x4c00
	s_addc_u32 s21, s95, 0
	s_add_u32 s22, s94, 0x4d00
	s_addc_u32 s23, s95, 0
	s_add_u32 s24, s94, 0x4e00
	s_addc_u32 s25, s95, 0
	s_add_u32 s26, s94, 0x4f00
	s_addc_u32 s27, s95, 0
	s_add_u32 s28, s94, 0x5000
	s_addc_u32 s29, s95, 0
	s_add_u32 s30, s94, 0x5100
	s_addc_u32 s31, s95, 0
	s_add_u32 s34, s94, 0x5200
	s_addc_u32 s35, s95, 0
	s_add_u32 s36, s94, 0x5300
	s_addc_u32 s37, s95, 0
	s_mov_b32 s44, 1
	v_mov_b32_e32 v16, 0
	s_branch .LBB0_577

.LBB0_904:
	s_cmp_gt_i32 s6, 9
	s_cselect_b64 s[0:1], -1, 0
	s_cmp_lt_i32 s7, 10
	s_cselect_b64 s[2:3], -1, 0
	s_or_b64 s[0:1], s[0:1], s[2:3]
	s_and_b64 vcc, exec, s[0:1]
	s_cbranch_vccnz .LBB0_1038
	s_mov_b32 s98, s88
	s_and_b32 s99, s88, 31
	s_lshl_b32 s99, s99, 3
	s_lshr_b32 s88, s88, 5
	s_or_b32 s88, s88, s99
	v_readlane_b32 s99, v253, 20
	s_nop 3
	s_cmp_lt_u32 s99, 4
	s_cbranch_scc1 .Lgprio_3
	s_setprio 1
.Lgprio_3:
	s_waitcnt vmcnt(0)
	v_mov_b32_e32 v1, 0x420000
	v_mbcnt_lo_u32_b32 v0, -1, 0
	v_mbcnt_hi_u32_b32 v0, -1, v0
	global_load_dword v1, v1, s[94:95]
	s_and_b32 s0, s89, 0xffffffc0
	s_movk_i32 s1, 0x140
	v_add_u32_e32 v0, s0, v0
	s_add_u32 s2, s94, 0x420000
	s_addc_u32 s3, s95, 0
	v_cmp_gt_i32_e32 vcc, s1, v0
	s_waitcnt vmcnt(0)
	v_readfirstlane_b32 s41, v1
	s_and_saveexec_b64 s[0:1], vcc
	s_cbranch_execz .LBB0_907
	v_ashrrev_i32_e32 v1, 31, v0
	v_lshl_add_u64 v[2:3], v[0:1], 2, s[2:3]
	global_load_dword v1, v[2:3], off offset:4
	v_lshl_add_u32 v2, v0, 2, 0
	v_add_u32_e32 v2, 0x22400, v2
	s_waitcnt vmcnt(0)
	ds_write_b32 v2, v1

.LBB0_988:
	v_readlane_b32 s6, v253, 23
	v_readlane_b32 s7, v253, 24
	s_mov_b32 s88, s98
	s_setprio 0
	s_cmp_lt_u32 s7, 11
	s_waitcnt vmcnt(0)
	s_barrier
	s_cbranch_scc1 .LBB0_1038
	v_readlane_b32 s0, v253, 20
	s_waitcnt vmcnt(0)
	s_lshl_b32 s0, s0, 6
	s_sub_i32 s0, 0, s0
	s_barrier
	v_mbcnt_lo_u32_b32 v0, -1, 0
	v_mbcnt_hi_u32_b32 v0, -1, v0
	s_nop 0
	v_cmp_eq_u32_e32 vcc, s0, v0
	s_and_saveexec_b64 s[0:1], vcc
	s_cbranch_execz .LBB0_1037
	s_add_i32 s2, 0, 0x20160
	v_mov_b32_e32 v0, s2
	s_waitcnt vmcnt(0) expcnt(0) lgkmcnt(0)
	ds_read_b32 v2, v0
	s_add_i32 s2, 0, 0x20164
	v_mov_b32_e32 v0, s2
	ds_read_b32 v0, v0
	s_waitcnt lgkmcnt(1)
	v_cmp_ne_u32_e32 vcc, 0, v2
	s_cbranch_vccnz .LBB0_1005
	v_readlane_b32 s2, v253, 0
	v_readlane_b32 s3, v253, 1
	s_load_dwordx2 s[6:7], s[2:3], 0x4
	s_add_u32 s2, s94, 0x4200
	s_addc_u32 s3, s95, 0
	s_add_u32 s4, s94, 0x4400
	s_addc_u32 s5, s95, 0
	s_waitcnt lgkmcnt(0)
	s_mul_i32 s33, s6, s90
	s_add_u32 s6, s94, 0x4500
	s_mul_i32 s33, s33, s7
	s_addc_u32 s7, s95, 0
	s_add_u32 s8, s94, 0x4600
	s_addc_u32 s9, s95, 0
	s_add_u32 s10, s94, 0x4700
	s_addc_u32 s11, s95, 0
	s_add_u32 s12, s94, 0x4800
	s_addc_u32 s13, s95, 0
	s_add_u32 s14, s94, 0x4900
	s_addc_u32 s15, s95, 0
	s_add_u32 s16, s94, 0x4a00
	s_addc_u32 s17, s95, 0
	s_add_u32 s18, s94, 0x4b00
	s_addc_u32 s19, s95, 0
	s_add_u32 s20, s94, 0x4c00
	s_addc_u32 s21, s95, 0
	s_add_u32 s22, s94, 0x4d00
	s_addc_u32 s23, s95, 0
	s_add_u32 s24, s94, 0x4e00
	s_addc_u32 s25, s95, 0
	s_add_u32 s26, s94, 0x4f00
	s_addc_u32 s27, s95, 0
	s_add_u32 s28, s94, 0x5000
	s_addc_u32 s29, s95, 0
	s_add_u32 s30, s94, 0x5100
	s_addc_u32 s31, s95, 0
	s_add_u32 s34, s94, 0x5200
	s_addc_u32 s35, s95, 0
	s_add_u32 s36, s94, 0x5300
	s_addc_u32 s37, s95, 0
	s_mov_b32 s44, 1
	v_mov_b32_e32 v16, 0
	s_branch .LBB0_993

.LBB0_1038:
	s_cmp_gt_i32 s6, 10
	s_cselect_b64 s[0:1], -1, 0
	s_cmp_lt_i32 s7, 11
	s_cselect_b64 s[2:3], -1, 0
	s_or_b64 s[0:1], s[0:1], s[2:3]
	s_and_b64 vcc, exec, s[0:1]
	s_cbranch_vccnz .LBB0_1136
	s_mov_b32 s98, s88
	s_and_b32 s99, s88, 31
	s_lshl_b32 s99, s99, 3
	s_lshr_b32 s88, s88, 5
	s_or_b32 s88, s88, s99
	v_readlane_b32 s99, v253, 20
	s_nop 3
	s_cmp_lt_u32 s99, 4
	s_cbranch_scc1 .Lgprio_4
	s_setprio 1
.Lgprio_4:
	s_waitcnt vmcnt(0)
	v_mov_b32_e32 v1, 0x420000
	v_mbcnt_lo_u32_b32 v0, -1, 0
	v_mbcnt_hi_u32_b32 v0, -1, v0
	global_load_dword v1, v1, s[94:95]
	s_and_b32 s0, s89, 0xffffffc0
	s_movk_i32 s1, 0x140
	v_add_u32_e32 v0, s0, v0
	s_add_u32 s2, s94, 0x420000
	s_addc_u32 s3, s95, 0
	v_cmp_gt_i32_e32 vcc, s1, v0
	s_waitcnt vmcnt(0)
	v_readfirstlane_b32 s44, v1
	s_and_saveexec_b64 s[0:1], vcc
	s_cbranch_execz .LBB0_1041
	v_ashrrev_i32_e32 v1, 31, v0
	v_lshl_add_u64 v[2:3], v[0:1], 2, s[2:3]
	global_load_dword v1, v[2:3], off offset:4
	v_lshl_add_u32 v0, v0, 2, 0
	v_add_u32_e32 v0, 0x22400, v0
	s_waitcnt vmcnt(0)
	ds_write_b32 v0, v1

.LBB0_1086:
	v_readlane_b32 s6, v253, 23
	v_readlane_b32 s7, v253, 24
	s_mov_b32 s88, s98
	s_setprio 0
	s_cmp_lt_u32 s7, 12
	s_waitcnt vmcnt(0)
	s_barrier
	s_cbranch_scc1 .LBB0_1136
	v_readlane_b32 s0, v253, 20
	s_waitcnt vmcnt(0)
	s_lshl_b32 s0, s0, 6
	s_sub_i32 s0, 0, s0
	s_barrier
	v_mbcnt_lo_u32_b32 v0, -1, 0
	v_mbcnt_hi_u32_b32 v0, -1, v0
	s_nop 0
	v_cmp_eq_u32_e32 vcc, s0, v0
	s_and_saveexec_b64 s[0:1], vcc
	s_cbranch_execz .LBB0_1135
	s_add_i32 s2, 0, 0x20160
	v_mov_b32_e32 v0, s2
	s_waitcnt vmcnt(0) expcnt(0) lgkmcnt(0)
	ds_read_b32 v2, v0
	s_add_i32 s2, 0, 0x20164
	v_mov_b32_e32 v0, s2
	ds_read_b32 v0, v0
	s_waitcnt lgkmcnt(1)
	v_cmp_ne_u32_e32 vcc, 0, v2
	s_cbranch_vccnz .LBB0_1103
	v_readlane_b32 s2, v253, 0
	v_readlane_b32 s3, v253, 1
	s_load_dwordx2 s[6:7], s[2:3], 0x4
	s_add_u32 s2, s94, 0x4200
	s_addc_u32 s3, s95, 0
	s_add_u32 s4, s94, 0x4400
	s_addc_u32 s5, s95, 0
	s_waitcnt lgkmcnt(0)
	s_mul_i32 s33, s6, s90
	s_add_u32 s6, s94, 0x4500
	s_mul_i32 s33, s33, s7
	s_addc_u32 s7, s95, 0
	s_add_u32 s8, s94, 0x4600
	s_addc_u32 s9, s95, 0
	s_add_u32 s10, s94, 0x4700
	s_addc_u32 s11, s95, 0
	s_add_u32 s12, s94, 0x4800
	s_addc_u32 s13, s95, 0
	s_add_u32 s14, s94, 0x4900
	s_addc_u32 s15, s95, 0
	s_add_u32 s16, s94, 0x4a00
	s_addc_u32 s17, s95, 0
	s_add_u32 s18, s94, 0x4b00
	s_addc_u32 s19, s95, 0
	s_add_u32 s20, s94, 0x4c00
	s_addc_u32 s21, s95, 0
	s_add_u32 s22, s94, 0x4d00
	s_addc_u32 s23, s95, 0
	s_add_u32 s24, s94, 0x4e00
	s_addc_u32 s25, s95, 0
	s_add_u32 s26, s94, 0x4f00
	s_addc_u32 s27, s95, 0
	s_add_u32 s28, s94, 0x5000
	s_addc_u32 s29, s95, 0
	s_add_u32 s30, s94, 0x5100
	s_addc_u32 s31, s95, 0
	s_add_u32 s34, s94, 0x5200
	s_addc_u32 s35, s95, 0
	s_add_u32 s36, s94, 0x5300
	s_addc_u32 s37, s95, 0
	s_mov_b32 s44, 1
	v_mov_b32_e32 v16, 0
	s_branch .LBB0_1091

.LBB0_1212:
	s_cmp_gt_i32 s6, 18
	s_cselect_b64 s[0:1], -1, 0
	s_cmp_lt_i32 s7, 19
	s_cselect_b64 s[2:3], -1, 0
	s_or_b64 s[0:1], s[0:1], s[2:3]
	s_and_b64 vcc, exec, s[0:1]
	s_cbranch_vccnz .LBB0_1297
	s_mov_b32 s98, s88
	s_and_b32 s99, s88, 31
	s_lshl_b32 s99, s99, 3
	s_lshr_b32 s88, s88, 5
	s_or_b32 s88, s88, s99
	v_readlane_b32 s99, v253, 20
	s_nop 3
	s_cmp_lt_u32 s99, 4
	s_cbranch_scc1 .Lgprio_5
	s_setprio 1
.Lgprio_5:
	s_and_b32 s0, s89, 0xffffffc0
	s_waitcnt vmcnt(0)
	v_mbcnt_lo_u32_b32 v0, -1, 0
	v_mbcnt_hi_u32_b32 v0, -1, v0
	s_nop 0
	v_add_u32_e32 v2, s0, v0
	s_movk_i32 s0, 0x800
	v_cmp_gt_i32_e32 vcc, s0, v2
	s_and_saveexec_b64 s[6:7], vcc
	s_cbranch_execz .LBB0_1220
	v_readlane_b32 s1, v253, 20
	s_lshl_b32 s0, s1, 8
	s_add_i32 s0, s0, 0
	v_lshl_add_u32 v1, v0, 2, s0
	v_lshlrev_b32_e32 v0, 1, v0
	v_add_u32_e32 v3, 0x20400, v1
	v_lshl_add_u32 v4, s1, 7, v0
	s_mov_b64 s[8:9], 0
	v_mov_b32_e32 v5, 0x461c4000
	s_mov_b32 s12, 0x3f2aaaab
	v_mov_b32_e32 v6, 0x3e91f4c4
	s_mov_b32 s13, 0x3f317218
	s_movk_i32 s14, 0x204
	s_mov_b32 s15, 0x7f800000
	s_mov_b32 s16, 0x42b17218
	v_mov_b32_e32 v7, 0x37000000
	s_mov_b32 s17, 0x3fb8aa3b
	s_mov_b32 s18, 0xc2ce8ed0
	v_mov_b32_e32 v8, 0x7f800000
	s_brev_b32 s19, 18
	s_mov_b32 s20, 0xfe5163ab
	v_mov_b32_e32 v1, 0
	s_mov_b32 s21, 0x3c439041
	s_mov_b32 s22, 0xdb629599
	s_mov_b32 s23, 0xf534ddc0
	s_mov_b32 s24, 0xfc2757d1
	s_mov_b32 s25, 0x4e441529
	s_mov_b32 s26, 0xa2f9836e
	s_mov_b32 s27, 0x3fc90fda
	s_mov_b32 s28, 0x3f22f983
	s_mov_b32 s29, 0xbfc90fda
	v_mov_b32_e32 v9, 0x3c0881c4
	v_mov_b32_e32 v10, 0xbab64f3b
	s_brev_b32 s30, 1
	s_movk_i32 s31, 0x1f8
	s_movk_i32 s33, 0x5ff
	v_not_b32_e32 v11, 63
	v_not_b32_e32 v12, 31
	v_mov_b32_e32 v13, 0x7fc00000
	s_branch .LBB0_1216

.LBB0_1247:
	v_readlane_b32 s6, v253, 23
	v_readlane_b32 s7, v253, 24
	s_mov_b32 s88, s98
	s_setprio 0
	s_cmp_gt_u32 s7, 19
	s_cbranch_scc0 .LBB0_1297
	v_readlane_b32 s0, v253, 20
	s_waitcnt vmcnt(0)
	s_lshl_b32 s0, s0, 6
	s_sub_i32 s0, 0, s0
	s_waitcnt vmcnt(0)
	s_barrier
	v_mbcnt_lo_u32_b32 v0, -1, 0
	v_mbcnt_hi_u32_b32 v0, -1, v0
	s_nop 0
	v_cmp_eq_u32_e32 vcc, s0, v0
	s_and_saveexec_b64 s[0:1], vcc
	s_cbranch_execz .LBB0_1296
	s_add_i32 s2, 0, 0x20160
	v_mov_b32_e32 v0, s2
	s_waitcnt vmcnt(0) expcnt(0) lgkmcnt(0)
	ds_read_b32 v2, v0
	s_add_i32 s2, 0, 0x20164
	v_mov_b32_e32 v0, s2
	ds_read_b32 v0, v0
	s_waitcnt lgkmcnt(1)
	v_cmp_ne_u32_e32 vcc, 0, v2
	s_cbranch_vccnz .LBB0_1264
	v_readlane_b32 s2, v253, 0
	v_readlane_b32 s3, v253, 1
	s_load_dwordx2 s[6:7], s[2:3], 0x4
	s_add_u32 s2, s94, 0x4200
	s_addc_u32 s3, s95, 0
	s_add_u32 s4, s94, 0x4400
	s_addc_u32 s5, s95, 0
	s_waitcnt lgkmcnt(0)
	s_mul_i32 s33, s6, s90
	s_add_u32 s6, s94, 0x4500
	s_mul_i32 s33, s33, s7
	s_addc_u32 s7, s95, 0
	s_add_u32 s8, s94, 0x4600
	s_addc_u32 s9, s95, 0
	s_add_u32 s10, s94, 0x4700
	s_addc_u32 s11, s95, 0
	s_add_u32 s12, s94, 0x4800
	s_addc_u32 s13, s95, 0
	s_add_u32 s14, s94, 0x4900
	s_addc_u32 s15, s95, 0
	s_add_u32 s16, s94, 0x4a00
	s_addc_u32 s17, s95, 0
	s_add_u32 s18, s94, 0x4b00
	s_addc_u32 s19, s95, 0
	s_add_u32 s20, s94, 0x4c00
	s_addc_u32 s21, s95, 0
	s_add_u32 s22, s94, 0x4d00
	s_addc_u32 s23, s95, 0
	s_add_u32 s24, s94, 0x4e00
	s_addc_u32 s25, s95, 0
	s_add_u32 s26, s94, 0x4f00
	s_addc_u32 s27, s95, 0
	s_add_u32 s28, s94, 0x5000
	s_addc_u32 s29, s95, 0
	s_add_u32 s30, s94, 0x5100
	s_addc_u32 s31, s95, 0
	s_add_u32 s34, s94, 0x5200
	s_addc_u32 s35, s95, 0
	s_add_u32 s36, s94, 0x5300
	s_addc_u32 s37, s95, 0
	s_mov_b32 s44, 1
	v_mov_b32_e32 v16, 0
	s_branch .LBB0_1252

.LBB0_1370:
	s_cmp_gt_i32 s6, 21
	s_cselect_b64 s[0:1], -1, 0
	s_cmp_lt_i32 s7, 22
	s_cselect_b64 s[2:3], -1, 0
	s_or_b64 s[0:1], s[0:1], s[2:3]
	s_and_b64 vcc, exec, s[0:1]
	s_cbranch_vccnz .LBB0_1445
	s_mov_b32 s98, s88
	s_and_b32 s99, s88, 31
	s_lshl_b32 s99, s99, 3
	s_lshr_b32 s88, s88, 5
	s_or_b32 s88, s88, s99
	v_readlane_b32 s99, v253, 20
	s_nop 3
	s_cmp_lt_u32 s99, 4
	s_cbranch_scc1 .Lgprio_6
	s_setprio 1
.Lgprio_6:
	s_cmpk_gt_i32 s88, 0xff
	s_waitcnt vmcnt(0)
	v_mbcnt_lo_u32_b32 v0, -1, 0
	v_mbcnt_hi_u32_b32 v0, -1, v0
	v_mbcnt_lo_u32_b32 v8, -1, 0
	v_mbcnt_hi_u32_b32 v8, -1, v8
	s_cbranch_scc1 .LBB0_1395
	s_ashr_i32 s28, s88, 31
	s_lshr_b32 s0, s28, 29
	s_add_i32 s3, s88, s0
	s_and_b32 s0, s3, -8
	s_sub_i32 s4, s88, s0
	s_cmp_gt_i32 s4, -1
	s_cbranch_scc0 .LBB0_1374
	s_lshl_b32 s2, s4, 5
	s_cbranch_execz .LBB0_1375
	s_branch .LBB0_1376

.LBB0_1395:
	v_readlane_b32 s6, v253, 23
	v_readlane_b32 s7, v253, 24
	s_mov_b32 s88, s98
	s_setprio 0
	s_cmp_lt_u32 s7, 23
	s_cbranch_scc1 .LBB0_1445
	v_readlane_b32 s0, v253, 20
	s_waitcnt vmcnt(0)
	s_lshl_b32 s0, s0, 6
	s_sub_i32 s0, 0, s0
	s_waitcnt vmcnt(0)
	s_barrier
	v_mbcnt_lo_u32_b32 v0, -1, 0
	v_mbcnt_hi_u32_b32 v0, -1, v0
	s_nop 0
	v_cmp_eq_u32_e32 vcc, s0, v0
	s_and_saveexec_b64 s[0:1], vcc
	s_cbranch_execz .LBB0_1444
	s_add_i32 s2, 0, 0x20160
	v_mov_b32_e32 v0, s2
	s_waitcnt vmcnt(0) expcnt(0) lgkmcnt(0)
	ds_read_b32 v2, v0
	s_add_i32 s2, 0, 0x20164
	v_mov_b32_e32 v0, s2
	ds_read_b32 v0, v0
	s_waitcnt lgkmcnt(1)
	v_cmp_ne_u32_e32 vcc, 0, v2
	s_cbranch_vccnz .LBB0_1412
	v_readlane_b32 s2, v253, 0
	v_readlane_b32 s3, v253, 1
	s_load_dwordx2 s[6:7], s[2:3], 0x4
	s_add_u32 s2, s94, 0x4200
	s_addc_u32 s3, s95, 0
	s_add_u32 s4, s94, 0x4400
	s_addc_u32 s5, s95, 0
	s_waitcnt lgkmcnt(0)
	s_mul_i32 s33, s6, s90
	s_add_u32 s6, s94, 0x4500
	s_mul_i32 s33, s33, s7
	s_addc_u32 s7, s95, 0
	s_add_u32 s8, s94, 0x4600
	s_addc_u32 s9, s95, 0
	s_add_u32 s10, s94, 0x4700
	s_addc_u32 s11, s95, 0
	s_add_u32 s12, s94, 0x4800
	s_addc_u32 s13, s95, 0
	s_add_u32 s14, s94, 0x4900
	s_addc_u32 s15, s95, 0
	s_add_u32 s16, s94, 0x4a00
	s_addc_u32 s17, s95, 0
	s_add_u32 s18, s94, 0x4b00
	s_addc_u32 s19, s95, 0
	s_add_u32 s20, s94, 0x4c00
	s_addc_u32 s21, s95, 0
	s_add_u32 s22, s94, 0x4d00
	s_addc_u32 s23, s95, 0
	s_add_u32 s24, s94, 0x4e00
	s_addc_u32 s25, s95, 0
	s_add_u32 s26, s94, 0x4f00
	s_addc_u32 s27, s95, 0
	s_add_u32 s28, s94, 0x5000
	s_addc_u32 s29, s95, 0
	s_add_u32 s30, s94, 0x5100
	s_addc_u32 s31, s95, 0
	s_add_u32 s34, s94, 0x5200
	s_addc_u32 s35, s95, 0
	s_add_u32 s36, s94, 0x5300
	s_addc_u32 s37, s95, 0
	s_mov_b32 s44, 1
	v_mov_b32_e32 v16, 0
	s_branch .LBB0_1400

.LBB0_1727:
	s_cmp_gt_i32 s6, 25
	s_cselect_b64 s[0:1], -1, 0
	s_cmp_lt_i32 s7, 26
	s_cselect_b64 s[2:3], -1, 0
	s_or_b64 s[0:1], s[0:1], s[2:3]
	s_and_b64 vcc, exec, s[0:1]
	s_cbranch_vccnz .LBB0_1861
	s_mov_b32 s98, s88
	s_and_b32 s99, s88, 31
	s_lshl_b32 s99, s99, 3
	s_lshr_b32 s88, s88, 5
	s_or_b32 s88, s88, s99
	v_readlane_b32 s99, v253, 20
	s_nop 3
	s_cmp_lt_u32 s99, 4
	s_cbranch_scc1 .Lgprio_7
	s_setprio 1

.LBB0_1811:
	v_readlane_b32 s6, v253, 23
	v_readlane_b32 s7, v253, 24
	s_mov_b32 s88, s98
	s_setprio 0
	s_cmp_lt_u32 s7, 27
	s_waitcnt vmcnt(0)
	s_barrier
	s_cbranch_scc1 .LBB0_1861
	v_readlane_b32 s0, v253, 20
	s_waitcnt vmcnt(0)
	s_lshl_b32 s0, s0, 6
	s_sub_i32 s0, 0, s0
	s_barrier
	v_mbcnt_lo_u32_b32 v0, -1, 0
	v_mbcnt_hi_u32_b32 v0, -1, v0
	s_nop 0
	v_cmp_eq_u32_e32 vcc, s0, v0
	s_and_saveexec_b64 s[0:1], vcc
	s_cbranch_execz .LBB0_1860
	s_add_i32 s2, 0, 0x20160
	v_mov_b32_e32 v0, s2
	s_waitcnt vmcnt(0) expcnt(0) lgkmcnt(0)
	ds_read_b32 v2, v0
	s_add_i32 s2, 0, 0x20164
	v_mov_b32_e32 v0, s2
	ds_read_b32 v0, v0
	s_waitcnt lgkmcnt(1)
	v_cmp_ne_u32_e32 vcc, 0, v2
	s_cbranch_vccnz .LBB0_1828
	v_readlane_b32 s2, v253, 0
	v_readlane_b32 s3, v253, 1
	s_load_dwordx2 s[6:7], s[2:3], 0x4
	s_add_u32 s2, s94, 0x4200
	s_addc_u32 s3, s95, 0
	s_add_u32 s4, s94, 0x4400
	s_addc_u32 s5, s95, 0
	s_waitcnt lgkmcnt(0)
	s_mul_i32 s33, s6, s90
	s_add_u32 s6, s94, 0x4500
	s_mul_i32 s33, s33, s7
	s_addc_u32 s7, s95, 0
	s_add_u32 s8, s94, 0x4600
	s_addc_u32 s9, s95, 0
	s_add_u32 s10, s94, 0x4700
	s_addc_u32 s11, s95, 0
	s_add_u32 s12, s94, 0x4800
	s_addc_u32 s13, s95, 0
	s_add_u32 s14, s94, 0x4900
	s_addc_u32 s15, s95, 0
	s_add_u32 s16, s94, 0x4a00
	s_addc_u32 s17, s95, 0
	s_add_u32 s18, s94, 0x4b00
	s_addc_u32 s19, s95, 0
	s_add_u32 s20, s94, 0x4c00
	s_addc_u32 s21, s95, 0
	s_add_u32 s22, s94, 0x4d00
	s_addc_u32 s23, s95, 0
	s_add_u32 s24, s94, 0x4e00
	s_addc_u32 s25, s95, 0
	s_add_u32 s26, s94, 0x4f00
	s_addc_u32 s27, s95, 0
	s_add_u32 s28, s94, 0x5000
	s_addc_u32 s29, s95, 0
	s_add_u32 s30, s94, 0x5100
	s_addc_u32 s31, s95, 0
	s_add_u32 s34, s94, 0x5200
	s_addc_u32 s35, s95, 0
	s_add_u32 s36, s94, 0x5300
	s_addc_u32 s37, s95, 0
	s_mov_b32 s44, 1
	v_mov_b32_e32 v16, 0
	s_branch .LBB0_1816

.LBB0_1861:
	s_cmp_gt_i32 s6, 26
	s_cselect_b64 s[0:1], -1, 0
	s_cmp_lt_i32 s7, 27
	s_cselect_b64 s[2:3], -1, 0
	s_or_b64 s[0:1], s[0:1], s[2:3]
	s_and_b64 vcc, exec, s[0:1]
	s_cbranch_vccnz .LBB0_1959
	s_mov_b32 s98, s88
	s_and_b32 s99, s88, 31
	s_lshl_b32 s99, s99, 3
	s_lshr_b32 s88, s88, 5
	s_or_b32 s88, s88, s99
	v_readlane_b32 s99, v253, 20
	s_nop 3
	s_cmp_lt_u32 s99, 4
	s_cbranch_scc1 .Lgprio_8
	s_setprio 1

.LBB0_1909:
	v_readlane_b32 s6, v253, 23
	v_readlane_b32 s7, v253, 24
	s_mov_b32 s88, s98
	s_setprio 0
	s_cmp_lt_u32 s7, 28
	s_waitcnt vmcnt(0)
	s_barrier
	s_cbranch_scc1 .LBB0_1959
	v_readlane_b32 s0, v253, 20
	s_waitcnt vmcnt(0)
	s_lshl_b32 s0, s0, 6
	s_sub_i32 s0, 0, s0
	s_barrier
	v_mbcnt_lo_u32_b32 v0, -1, 0
	v_mbcnt_hi_u32_b32 v0, -1, v0
	s_nop 0
	v_cmp_eq_u32_e32 vcc, s0, v0
	s_and_saveexec_b64 s[0:1], vcc
	s_cbranch_execz .LBB0_1958
	s_add_i32 s2, 0, 0x20160
	v_mov_b32_e32 v0, s2
	s_waitcnt vmcnt(0) expcnt(0) lgkmcnt(0)
	ds_read_b32 v2, v0
	s_add_i32 s2, 0, 0x20164
	v_mov_b32_e32 v0, s2
	ds_read_b32 v0, v0
	s_waitcnt lgkmcnt(1)
	v_cmp_ne_u32_e32 vcc, 0, v2
	s_cbranch_vccnz .LBB0_1926
	v_readlane_b32 s2, v253, 0
	v_readlane_b32 s3, v253, 1
	s_load_dwordx2 s[6:7], s[2:3], 0x4
	s_add_u32 s2, s94, 0x4200
	s_addc_u32 s3, s95, 0
	s_add_u32 s4, s94, 0x4400
	s_addc_u32 s5, s95, 0
	s_waitcnt lgkmcnt(0)
	s_mul_i32 s33, s6, s90
	s_add_u32 s6, s94, 0x4500
	s_mul_i32 s33, s33, s7
	s_addc_u32 s7, s95, 0
	s_add_u32 s8, s94, 0x4600
	s_addc_u32 s9, s95, 0
	s_add_u32 s10, s94, 0x4700
	s_addc_u32 s11, s95, 0
	s_add_u32 s12, s94, 0x4800
	s_addc_u32 s13, s95, 0
	s_add_u32 s14, s94, 0x4900
	s_addc_u32 s15, s95, 0
	s_add_u32 s16, s94, 0x4a00
	s_addc_u32 s17, s95, 0
	s_add_u32 s18, s94, 0x4b00
	s_addc_u32 s19, s95, 0
	s_add_u32 s20, s94, 0x4c00
	s_addc_u32 s21, s95, 0
	s_add_u32 s22, s94, 0x4d00
	s_addc_u32 s23, s95, 0
	s_add_u32 s24, s94, 0x4e00
	s_addc_u32 s25, s95, 0
	s_add_u32 s26, s94, 0x4f00
	s_addc_u32 s27, s95, 0
	s_add_u32 s28, s94, 0x5000
	s_addc_u32 s29, s95, 0
	s_add_u32 s30, s94, 0x5100
	s_addc_u32 s31, s95, 0
	s_add_u32 s34, s94, 0x5200
	s_addc_u32 s35, s95, 0
	s_add_u32 s36, s94, 0x5300
	s_addc_u32 s37, s95, 0
	s_mov_b32 s44, 1
	v_mov_b32_e32 v16, 0
	s_branch .LBB0_1914

.LBB0_2038:
	s_cmp_gt_i32 s6, 34
	s_cselect_b64 s[0:1], -1, 0
	s_cmp_lt_i32 s7, 35
	s_cselect_b64 s[2:3], -1, 0
	s_or_b64 s[0:1], s[0:1], s[2:3]
	s_and_b64 vcc, exec, s[0:1]
	s_cbranch_vccnz .LBB0_2128
	s_mov_b32 s98, s88
	s_and_b32 s99, s88, 31
	s_lshl_b32 s99, s99, 3
	s_lshr_b32 s88, s88, 5
	s_or_b32 s88, s88, s99
	v_readlane_b32 s99, v253, 20
	s_nop 3
	s_cmp_lt_u32 s99, 4
	s_cbranch_scc1 .Lgprio_9
	s_setprio 1
.Lgprio_9:
	s_add_u32 s6, s94, 0x4a600000
	s_addc_u32 s7, s95, 0
	s_cmpk_lt_i32 s88, 0x100
	v_mbcnt_lo_u32_b32 v144, -1, 0
	v_mbcnt_hi_u32_b32 v144, -1, v144
	s_waitcnt vmcnt(0)
	v_mbcnt_lo_u32_b32 v8, -1, 0
	v_mbcnt_hi_u32_b32 v8, -1, v8
	s_cbranch_scc1 .LBB0_2041
	s_ashr_i32 s43, s90, 31
	s_mov_b32 s42, 0
	s_cbranch_execz .LBB0_2042
	s_branch .LBB0_2065

.LBB0_2078:
	v_readlane_b32 s6, v253, 23
	v_readlane_b32 s7, v253, 24
	s_mov_b32 s88, s98
	s_setprio 0
	s_cmp_gt_u32 s7, 35
	s_cbranch_scc0 .LBB0_2128
	v_readlane_b32 s0, v253, 20
	s_waitcnt vmcnt(0)
	s_lshl_b32 s0, s0, 6
	s_sub_i32 s0, 0, s0
	s_waitcnt vmcnt(63) expcnt(7) lgkmcnt(15)
	s_barrier
	v_mbcnt_lo_u32_b32 v0, -1, 0
	v_mbcnt_hi_u32_b32 v0, -1, v0
	s_nop 0
	v_cmp_eq_u32_e32 vcc, s0, v0
	s_and_saveexec_b64 s[0:1], vcc
	s_cbranch_execz .LBB0_2127
	s_add_i32 s2, 0, 0x20160
	v_mov_b32_e32 v0, s2
	s_waitcnt vmcnt(0) expcnt(0) lgkmcnt(0)
	ds_read_b32 v2, v0
	s_add_i32 s2, 0, 0x20164
	v_mov_b32_e32 v0, s2
	ds_read_b32 v0, v0
	s_waitcnt lgkmcnt(1)
	v_cmp_ne_u32_e32 vcc, 0, v2
	s_cbranch_vccnz .LBB0_2095
	v_readlane_b32 s2, v253, 0
	v_readlane_b32 s3, v253, 1
	s_load_dwordx2 s[6:7], s[2:3], 0x4
	s_add_u32 s2, s94, 0x4200
	s_addc_u32 s3, s95, 0
	s_add_u32 s4, s94, 0x4400
	s_addc_u32 s5, s95, 0
	s_waitcnt lgkmcnt(0)
	s_mul_i32 s33, s6, s90
	s_add_u32 s6, s94, 0x4500
	s_mul_i32 s33, s33, s7
	s_addc_u32 s7, s95, 0
	s_add_u32 s8, s94, 0x4600
	s_addc_u32 s9, s95, 0
	s_add_u32 s10, s94, 0x4700
	s_addc_u32 s11, s95, 0
	s_add_u32 s12, s94, 0x4800
	s_addc_u32 s13, s95, 0
	s_add_u32 s14, s94, 0x4900
	s_addc_u32 s15, s95, 0
	s_add_u32 s16, s94, 0x4a00
	s_addc_u32 s17, s95, 0
	s_add_u32 s18, s94, 0x4b00
	s_addc_u32 s19, s95, 0
	s_add_u32 s20, s94, 0x4c00
	s_addc_u32 s21, s95, 0
	s_add_u32 s22, s94, 0x4d00
	s_addc_u32 s23, s95, 0
	s_add_u32 s24, s94, 0x4e00
	s_addc_u32 s25, s95, 0
	s_add_u32 s26, s94, 0x4f00
	s_addc_u32 s27, s95, 0
	s_add_u32 s28, s94, 0x5000
	s_addc_u32 s29, s95, 0
	s_add_u32 s30, s94, 0x5100
	s_addc_u32 s31, s95, 0
	s_add_u32 s34, s94, 0x5200
	s_addc_u32 s35, s95, 0
	s_add_u32 s36, s94, 0x5300
	s_addc_u32 s37, s95, 0
	s_mov_b32 s44, 1
	v_mov_b32_e32 v16, 0
	s_branch .LBB0_2083

.LBB0_2128:
	s_cmp_gt_i32 s6, 36
	s_cselect_b64 s[0:1], -1, 0
	s_cmp_lt_i32 s7, 37
	s_cselect_b64 s[2:3], -1, 0
	s_or_b64 s[0:1], s[0:1], s[2:3]
	s_and_b64 vcc, exec, s[0:1]
	s_cbranch_vccnz .LBB0_2203
	s_mov_b32 s98, s88
	s_and_b32 s99, s88, 31
	s_lshl_b32 s99, s99, 3
	s_lshr_b32 s88, s88, 5
	s_or_b32 s88, s88, s99
	v_readlane_b32 s99, v253, 20
	s_nop 3
	s_cmp_lt_u32 s99, 4
	s_cbranch_scc1 .Lgprio_10
	s_setprio 1

.LBB0_2153:
	v_readlane_b32 s6, v253, 23
	v_readlane_b32 s7, v253, 24
	s_mov_b32 s88, s98
	s_setprio 0
	s_cmp_lt_u32 s7, 38
	s_cbranch_scc1 .LBB0_2203
	v_readlane_b32 s0, v253, 20
	s_waitcnt vmcnt(0)
	s_lshl_b32 s0, s0, 6
	s_sub_i32 s0, 0, s0
	s_waitcnt vmcnt(0)
	s_barrier
	v_mbcnt_lo_u32_b32 v0, -1, 0
	v_mbcnt_hi_u32_b32 v0, -1, v0
	s_nop 0
	v_cmp_eq_u32_e32 vcc, s0, v0
	s_and_saveexec_b64 s[0:1], vcc
	s_cbranch_execz .LBB0_2202
	s_add_i32 s2, 0, 0x20160
	v_mov_b32_e32 v0, s2
	s_waitcnt vmcnt(0) expcnt(0) lgkmcnt(0)
	ds_read_b32 v2, v0
	s_add_i32 s2, 0, 0x20164
	v_mov_b32_e32 v0, s2
	ds_read_b32 v0, v0
	s_waitcnt lgkmcnt(1)
	v_cmp_ne_u32_e32 vcc, 0, v2
	s_cbranch_vccnz .LBB0_2170
	v_readlane_b32 s2, v253, 0
	v_readlane_b32 s3, v253, 1
	s_load_dwordx2 s[6:7], s[2:3], 0x4
	s_add_u32 s2, s94, 0x4200
	s_addc_u32 s3, s95, 0
	s_add_u32 s4, s94, 0x4400
	s_addc_u32 s5, s95, 0
	s_waitcnt lgkmcnt(0)
	s_mul_i32 s33, s6, s90
	s_add_u32 s6, s94, 0x4500
	s_mul_i32 s33, s33, s7
	s_addc_u32 s7, s95, 0
	s_add_u32 s8, s94, 0x4600
	s_addc_u32 s9, s95, 0
	s_add_u32 s10, s94, 0x4700
	s_addc_u32 s11, s95, 0
	s_add_u32 s12, s94, 0x4800
	s_addc_u32 s13, s95, 0
	s_add_u32 s14, s94, 0x4900
	s_addc_u32 s15, s95, 0
	s_add_u32 s16, s94, 0x4a00
	s_addc_u32 s17, s95, 0
	s_add_u32 s18, s94, 0x4b00
	s_addc_u32 s19, s95, 0
	s_add_u32 s20, s94, 0x4c00
	s_addc_u32 s21, s95, 0
	s_add_u32 s22, s94, 0x4d00
	s_addc_u32 s23, s95, 0
	s_add_u32 s24, s94, 0x4e00
	s_addc_u32 s25, s95, 0
	s_add_u32 s26, s94, 0x4f00
	s_addc_u32 s27, s95, 0
	s_add_u32 s28, s94, 0x5000
	s_addc_u32 s29, s95, 0
	s_add_u32 s30, s94, 0x5100
	s_addc_u32 s31, s95, 0
	s_add_u32 s34, s94, 0x5200
	s_addc_u32 s35, s95, 0
	s_add_u32 s36, s94, 0x5300
	s_addc_u32 s37, s95, 0
	s_mov_b32 s44, 1
	v_mov_b32_e32 v16, 0
	s_branch .LBB0_2158

.LBB0_2203:
	s_cmp_gt_i32 s6, 37
	s_cselect_b64 s[0:1], -1, 0
	s_cmp_lt_i32 s7, 38
	s_cselect_b64 s[2:3], -1, 0
	s_or_b64 s[0:1], s[0:1], s[2:3]
	s_and_b64 vcc, exec, s[0:1]
	s_cbranch_vccnz .LBB0_2278
	s_mov_b32 s98, s88
	s_and_b32 s99, s88, 31
	s_lshl_b32 s99, s99, 3
	s_lshr_b32 s88, s88, 5
	s_or_b32 s88, s88, s99
	v_readlane_b32 s99, v253, 20
	s_nop 3
	s_cmp_lt_u32 s99, 4
	s_cbranch_scc1 .Lgprio_11
	s_setprio 1
.Lgprio_11:
	s_cmpk_gt_i32 s88, 0xff
	s_waitcnt vmcnt(0)
	v_mbcnt_lo_u32_b32 v0, -1, 0
	v_mbcnt_hi_u32_b32 v0, -1, v0
	v_mbcnt_lo_u32_b32 v8, -1, 0
	v_mbcnt_hi_u32_b32 v8, -1, v8
	s_cbranch_scc1 .LBB0_2228
	s_ashr_i32 s30, s88, 31
	s_lshr_b32 s0, s30, 29
	s_add_i32 s2, s88, s0
	s_and_b32 s0, s2, -8
	s_sub_i32 s3, s88, s0
	s_cmp_gt_i32 s3, -1
	s_cbranch_scc0 .LBB0_2207
	s_lshl_b32 s4, s3, 5
	s_cbranch_execz .LBB0_2208
	s_branch .LBB0_2209

.LBB0_2228:
	v_readlane_b32 s6, v253, 23
	v_readlane_b32 s7, v253, 24
	s_mov_b32 s88, s98
	s_setprio 0
	s_cmp_lt_u32 s7, 39
	s_cbranch_scc1 .LBB0_2278
	v_readlane_b32 s0, v253, 20
	s_waitcnt vmcnt(0)
	s_lshl_b32 s0, s0, 6
	s_sub_i32 s0, 0, s0
	s_barrier
	v_mbcnt_lo_u32_b32 v0, -1, 0
	v_mbcnt_hi_u32_b32 v0, -1, v0
	s_nop 0
	v_cmp_eq_u32_e32 vcc, s0, v0
	s_and_saveexec_b64 s[0:1], vcc
	s_cbranch_execz .LBB0_2277
	s_add_i32 s2, 0, 0x20160
	v_mov_b32_e32 v0, s2
	s_waitcnt vmcnt(0) expcnt(0) lgkmcnt(0)
	ds_read_b32 v2, v0
	s_add_i32 s2, 0, 0x20164
	v_mov_b32_e32 v0, s2
	ds_read_b32 v0, v0
	s_waitcnt lgkmcnt(1)
	v_cmp_ne_u32_e32 vcc, 0, v2
	s_cbranch_vccnz .LBB0_2245
	v_readlane_b32 s2, v253, 0
	v_readlane_b32 s3, v253, 1
	s_load_dwordx2 s[6:7], s[2:3], 0x4
	s_add_u32 s2, s94, 0x4200
	s_addc_u32 s3, s95, 0
	s_add_u32 s4, s94, 0x4400
	s_addc_u32 s5, s95, 0
	s_waitcnt lgkmcnt(0)
	s_mul_i32 s33, s6, s90
	s_add_u32 s6, s94, 0x4500
	s_mul_i32 s33, s33, s7
	s_addc_u32 s7, s95, 0
	s_add_u32 s8, s94, 0x4600
	s_addc_u32 s9, s95, 0
	s_add_u32 s10, s94, 0x4700
	s_addc_u32 s11, s95, 0
	s_add_u32 s12, s94, 0x4800
	s_addc_u32 s13, s95, 0
	s_add_u32 s14, s94, 0x4900
	s_addc_u32 s15, s95, 0
	s_add_u32 s16, s94, 0x4a00
	s_addc_u32 s17, s95, 0
	s_add_u32 s18, s94, 0x4b00
	s_addc_u32 s19, s95, 0
	s_add_u32 s20, s94, 0x4c00
	s_addc_u32 s21, s95, 0
	s_add_u32 s22, s94, 0x4d00
	s_addc_u32 s23, s95, 0
	s_add_u32 s24, s94, 0x4e00
	s_addc_u32 s25, s95, 0
	s_add_u32 s26, s94, 0x4f00
	s_addc_u32 s27, s95, 0
	s_add_u32 s28, s94, 0x5000
	s_addc_u32 s29, s95, 0
	s_add_u32 s30, s94, 0x5100
	s_addc_u32 s31, s95, 0
	s_add_u32 s34, s94, 0x5200
	s_addc_u32 s35, s95, 0
	s_add_u32 s36, s94, 0x5300
	s_addc_u32 s37, s95, 0
	s_mov_b32 s44, 1
	v_mov_b32_e32 v16, 0
	s_branch .LBB0_2233

.LBB0_2278:
	s_cmp_gt_i32 s6, 38
	s_cselect_b64 s[0:1], -1, 0
	s_cmp_lt_i32 s7, 39
	s_cselect_b64 s[2:3], -1, 0
	s_or_b64 s[0:1], s[0:1], s[2:3]
	s_and_b64 vcc, exec, s[0:1]
	s_cbranch_vccnz .LBB0_2353
	s_mov_b32 s98, s88
	s_and_b32 s99, s88, 31
	s_lshl_b32 s99, s99, 3
	s_lshr_b32 s88, s88, 5
	s_or_b32 s88, s88, s99
	v_readlane_b32 s99, v253, 20
	s_nop 3
	s_cmp_lt_u32 s99, 4
	s_cbranch_scc1 .Lgprio_12
	s_setprio 1

.LBB0_2303:
	v_readlane_b32 s6, v253, 23
	v_readlane_b32 s7, v253, 24
	s_mov_b32 s88, s98
	s_setprio 0
	s_cmp_lt_u32 s7, 40
	s_cbranch_scc1 .LBB0_2353
	v_readlane_b32 s0, v253, 20
	s_waitcnt vmcnt(0)
	s_lshl_b32 s0, s0, 6
	s_sub_i32 s0, 0, s0
	s_waitcnt vmcnt(0)
	s_barrier
	v_mbcnt_lo_u32_b32 v0, -1, 0
	v_mbcnt_hi_u32_b32 v0, -1, v0
	s_nop 0
	v_cmp_eq_u32_e32 vcc, s0, v0
	s_and_saveexec_b64 s[0:1], vcc
	s_cbranch_execz .LBB0_2352
	s_add_i32 s2, 0, 0x20160
	v_mov_b32_e32 v0, s2
	s_waitcnt vmcnt(0) expcnt(0) lgkmcnt(0)
	ds_read_b32 v2, v0
	s_add_i32 s2, 0, 0x20164
	v_mov_b32_e32 v0, s2
	ds_read_b32 v0, v0
	s_waitcnt lgkmcnt(1)
	v_cmp_ne_u32_e32 vcc, 0, v2
	s_cbranch_vccnz .LBB0_2320
	v_readlane_b32 s2, v253, 0
	v_readlane_b32 s3, v253, 1
	s_load_dwordx2 s[6:7], s[2:3], 0x4
	s_add_u32 s2, s94, 0x4200
	s_addc_u32 s3, s95, 0
	s_add_u32 s4, s94, 0x4400
	s_addc_u32 s5, s95, 0
	s_waitcnt lgkmcnt(0)
	s_mul_i32 s33, s6, s90
	s_add_u32 s6, s94, 0x4500
	s_mul_i32 s33, s33, s7
	s_addc_u32 s7, s95, 0
	s_add_u32 s8, s94, 0x4600
	s_addc_u32 s9, s95, 0
	s_add_u32 s10, s94, 0x4700
	s_addc_u32 s11, s95, 0
	s_add_u32 s12, s94, 0x4800
	s_addc_u32 s13, s95, 0
	s_add_u32 s14, s94, 0x4900
	s_addc_u32 s15, s95, 0
	s_add_u32 s16, s94, 0x4a00
	s_addc_u32 s17, s95, 0
	s_add_u32 s18, s94, 0x4b00
	s_addc_u32 s19, s95, 0
	s_add_u32 s20, s94, 0x4c00
	s_addc_u32 s21, s95, 0
	s_add_u32 s22, s94, 0x4d00
	s_addc_u32 s23, s95, 0
	s_add_u32 s24, s94, 0x4e00
	s_addc_u32 s25, s95, 0
	s_add_u32 s26, s94, 0x4f00
	s_addc_u32 s27, s95, 0
	s_add_u32 s28, s94, 0x5000
	s_addc_u32 s29, s95, 0
	s_add_u32 s30, s94, 0x5100
	s_addc_u32 s31, s95, 0
	s_add_u32 s34, s94, 0x5200
	s_addc_u32 s35, s95, 0
	s_add_u32 s36, s94, 0x5300
	s_addc_u32 s37, s95, 0
	s_mov_b32 s44, 1
	v_mov_b32_e32 v16, 0
	s_branch .LBB0_2308

.LBB0_2635:
	s_cmp_gt_i32 s6, 41
	s_cselect_b64 s[0:1], -1, 0
	s_cmp_lt_i32 s7, 42
	s_cselect_b64 s[2:3], -1, 0
	s_or_b64 s[0:1], s[0:1], s[2:3]
	s_and_b64 vcc, exec, s[0:1]
	s_cbranch_vccnz .LBB0_2769
	s_mov_b32 s98, s88
	s_and_b32 s99, s88, 31
	s_lshl_b32 s99, s99, 3
	s_lshr_b32 s88, s88, 5
	s_or_b32 s88, s88, s99
	v_readlane_b32 s99, v253, 20
	s_nop 3
	s_cmp_lt_u32 s99, 4
	s_cbranch_scc1 .Lgprio_13
	s_setprio 1

.LBB0_2719:
	v_readlane_b32 s6, v253, 23
	v_readlane_b32 s7, v253, 24
	s_mov_b32 s88, s98
	s_setprio 0
	s_cmp_lt_u32 s7, 43
	s_waitcnt vmcnt(0)
	s_barrier
	s_cbranch_scc1 .LBB0_2769
	v_readlane_b32 s0, v253, 20
	s_waitcnt vmcnt(0)
	s_lshl_b32 s0, s0, 6
	s_sub_i32 s0, 0, s0
	s_barrier
	v_mbcnt_lo_u32_b32 v0, -1, 0
	v_mbcnt_hi_u32_b32 v0, -1, v0
	s_nop 0
	v_cmp_eq_u32_e32 vcc, s0, v0
	s_and_saveexec_b64 s[0:1], vcc
	s_cbranch_execz .LBB0_2768
	s_add_i32 s2, 0, 0x20160
	v_mov_b32_e32 v0, s2
	s_waitcnt vmcnt(0) expcnt(0) lgkmcnt(0)
	ds_read_b32 v2, v0
	s_add_i32 s2, 0, 0x20164
	v_mov_b32_e32 v0, s2
	ds_read_b32 v0, v0
	s_waitcnt lgkmcnt(1)
	v_cmp_ne_u32_e32 vcc, 0, v2
	s_cbranch_vccnz .LBB0_2736
	v_readlane_b32 s2, v253, 0
	v_readlane_b32 s3, v253, 1
	s_load_dwordx2 s[6:7], s[2:3], 0x4
	s_add_u32 s2, s94, 0x4200
	s_addc_u32 s3, s95, 0
	s_add_u32 s4, s94, 0x4400
	s_addc_u32 s5, s95, 0
	s_waitcnt lgkmcnt(0)
	s_mul_i32 s33, s6, s90
	s_add_u32 s6, s94, 0x4500
	s_mul_i32 s33, s33, s7
	s_addc_u32 s7, s95, 0
	s_add_u32 s8, s94, 0x4600
	s_addc_u32 s9, s95, 0
	s_add_u32 s10, s94, 0x4700
	s_addc_u32 s11, s95, 0
	s_add_u32 s12, s94, 0x4800
	s_addc_u32 s13, s95, 0
	s_add_u32 s14, s94, 0x4900
	s_addc_u32 s15, s95, 0
	s_add_u32 s16, s94, 0x4a00
	s_addc_u32 s17, s95, 0
	s_add_u32 s18, s94, 0x4b00
	s_addc_u32 s19, s95, 0
	s_add_u32 s20, s94, 0x4c00
	s_addc_u32 s21, s95, 0
	s_add_u32 s22, s94, 0x4d00
	s_addc_u32 s23, s95, 0
	s_add_u32 s24, s94, 0x4e00
	s_addc_u32 s25, s95, 0
	s_add_u32 s26, s94, 0x4f00
	s_addc_u32 s27, s95, 0
	s_add_u32 s28, s94, 0x5000
	s_addc_u32 s29, s95, 0
	s_add_u32 s30, s94, 0x5100
	s_addc_u32 s31, s95, 0
	s_add_u32 s34, s94, 0x5200
	s_addc_u32 s35, s95, 0
	s_add_u32 s36, s94, 0x5300
	s_addc_u32 s37, s95, 0
	s_mov_b32 s44, 1
	v_mov_b32_e32 v16, 0
	s_branch .LBB0_2724

.LBB0_2769:
	s_cmp_gt_i32 s6, 42
	s_cselect_b64 s[0:1], -1, 0
	s_cmp_lt_i32 s7, 43
	s_cselect_b64 s[2:3], -1, 0
	s_or_b64 s[0:1], s[0:1], s[2:3]
	s_and_b64 vcc, exec, s[0:1]
	s_cbranch_vccnz .LBB0_2867
	s_mov_b32 s98, s88
	s_and_b32 s99, s88, 31
	s_lshl_b32 s99, s99, 3
	s_lshr_b32 s88, s88, 5
	s_or_b32 s88, s88, s99
	v_readlane_b32 s99, v253, 20
	s_nop 3
	s_cmp_lt_u32 s99, 4
	s_cbranch_scc1 .Lgprio_14
	s_setprio 1

.LBB0_2817:
	v_readlane_b32 s6, v253, 23
	v_readlane_b32 s7, v253, 24
	s_mov_b32 s88, s98
	s_setprio 0
	s_cmp_lt_u32 s7, 44
	s_waitcnt vmcnt(0)
	s_barrier
	s_cbranch_scc1 .LBB0_2867
	v_readlane_b32 s0, v253, 20
	s_waitcnt vmcnt(0)
	s_lshl_b32 s0, s0, 6
	s_sub_i32 s0, 0, s0
	s_barrier
	v_mbcnt_lo_u32_b32 v0, -1, 0
	v_mbcnt_hi_u32_b32 v0, -1, v0
	s_nop 0
	v_cmp_eq_u32_e32 vcc, s0, v0
	s_and_saveexec_b64 s[0:1], vcc
	s_cbranch_execz .LBB0_2866
	s_add_i32 s2, 0, 0x20160
	v_mov_b32_e32 v0, s2
	s_waitcnt vmcnt(0) expcnt(0) lgkmcnt(0)
	ds_read_b32 v2, v0
	s_add_i32 s2, 0, 0x20164
	v_mov_b32_e32 v0, s2
	ds_read_b32 v0, v0
	s_waitcnt lgkmcnt(1)
	v_cmp_ne_u32_e32 vcc, 0, v2
	s_cbranch_vccnz .LBB0_2834
	v_readlane_b32 s2, v253, 0
	v_readlane_b32 s3, v253, 1
	s_load_dwordx2 s[6:7], s[2:3], 0x4
	s_add_u32 s2, s94, 0x4200
	s_addc_u32 s3, s95, 0
	s_add_u32 s4, s94, 0x4400
	s_addc_u32 s5, s95, 0
	s_waitcnt lgkmcnt(0)
	s_mul_i32 s33, s6, s90
	s_add_u32 s6, s94, 0x4500
	s_mul_i32 s33, s33, s7
	s_addc_u32 s7, s95, 0
	s_add_u32 s8, s94, 0x4600
	s_addc_u32 s9, s95, 0
	s_add_u32 s10, s94, 0x4700
	s_addc_u32 s11, s95, 0
	s_add_u32 s12, s94, 0x4800
	s_addc_u32 s13, s95, 0
	s_add_u32 s14, s94, 0x4900
	s_addc_u32 s15, s95, 0
	s_add_u32 s16, s94, 0x4a00
	s_addc_u32 s17, s95, 0
	s_add_u32 s18, s94, 0x4b00
	s_addc_u32 s19, s95, 0
	s_add_u32 s20, s94, 0x4c00
	s_addc_u32 s21, s95, 0
	s_add_u32 s22, s94, 0x4d00
	s_addc_u32 s23, s95, 0
	s_add_u32 s24, s94, 0x4e00
	s_addc_u32 s25, s95, 0
	s_add_u32 s26, s94, 0x4f00
	s_addc_u32 s27, s95, 0
	s_add_u32 s28, s94, 0x5000
	s_addc_u32 s29, s95, 0
	s_add_u32 s30, s94, 0x5100
	s_addc_u32 s31, s95, 0
	s_add_u32 s34, s94, 0x5200
	s_addc_u32 s35, s95, 0
	s_add_u32 s36, s94, 0x5300
	s_addc_u32 s37, s95, 0
	s_mov_b32 s44, 1
	v_mov_b32_e32 v16, 0
	s_branch .LBB0_2822

.LBB0_2943:
	s_cmp_gt_i32 s6, 50
	s_cselect_b64 s[0:1], -1, 0
	s_cmp_lt_i32 s7, 51
	s_cselect_b64 s[2:3], -1, 0
	s_or_b64 s[0:1], s[0:1], s[2:3]
	s_and_b64 vcc, exec, s[0:1]
	s_cbranch_vccnz .LBB0_3010
	s_mov_b32 s98, s88
	s_and_b32 s99, s88, 31
	s_lshl_b32 s99, s99, 3
	s_lshr_b32 s88, s88, 5
	s_or_b32 s88, s88, s99
	v_readlane_b32 s99, v253, 20
	s_nop 3
	s_cmp_lt_u32 s99, 4
	s_cbranch_scc1 .Lgprio_15
	s_setprio 1
.Lgprio_15:
	s_cmpk_gt_i32 s88, 0x4ff
	s_waitcnt vmcnt(0)
	v_mbcnt_lo_u32_b32 v0, -1, 0
	v_mbcnt_hi_u32_b32 v0, -1, v0
	v_mbcnt_lo_u32_b32 v6, -1, 0
	v_mbcnt_hi_u32_b32 v6, -1, v6
	s_cbranch_scc1 .LBB0_2960
	s_add_u32 s11, s94, 0x37600000
	s_addc_u32 s30, s95, 0
	s_add_u32 s31, s94, 0x1200000
	v_readlane_b32 s0, v253, 20
	s_addc_u32 s34, s95, 0
	s_lshl_b32 s35, s0, 10
	v_lshl_add_u32 v0, v6, 4, s35
	v_add_u32_e32 v1, 0x2000, v0
	v_ashrrev_i32_e32 v2, 31, v1
	v_lshrrev_b32_e32 v2, 22, v2
	v_add_u32_e32 v2, v1, v2
	v_ashrrev_i32_e32 v4, 10, v2
	v_mul_i32_i24_e32 v2, 0x400, v4
	v_sub_u32_e32 v1, v1, v2
	v_lshrrev_b32_e32 v2, 4, v1
	v_bitop3_b32 v1, v2, v1, 32 bitop3:0x6c
	v_ashrrev_i32_e32 v2, 31, v1
	v_lshrrev_b32_e32 v2, 26, v2
	v_add_u32_e32 v2, v1, v2
	v_ashrrev_i32_e32 v5, 6, v2
	v_lshlrev_b32_e32 v3, 3, v4
	v_and_b32_e32 v2, 0xffc0, v2
	v_and_b32_e32 v3, -16, v3
	v_sub_u32_e32 v1, v1, v2
	v_add_u32_e32 v3, v5, v3
	v_lshrrev_b16_e32 v2, 7, v1
	v_and_b32_e32 v7, 3, v5
	s_mov_b32 s0, 0x1ffffe0
	v_lshrrev_b32_e32 v8, 2, v3
	v_lshlrev_b32_e32 v9, 1, v3
	v_and_b32_e32 v2, 1, v2
	v_and_or_b32 v7, v3, s0, v7
	v_and_b32_e32 v8, 4, v8
	v_and_b32_e32 v9, 24, v9
	v_add_u16_e32 v1, v1, v2
	v_mov_b32_e32 v2, 1
	v_or3_b32 v8, v7, v8, v9
	v_lshlrev_b32_e32 v7, 5, v4
	v_ashrrev_i16_sdwa v1, v2, sext(v1) dst_sel:DWORD dst_unused:UNUSED_PAD src0_sel:DWORD src1_sel:BYTE_0
	v_and_b32_e32 v9, 32, v7
	v_bfe_i32 v7, v1, 0, 16
	v_add_lshl_u32 v1, v9, v7, 1
	v_lshl_add_u32 v160, v8, 7, v1
	v_lshl_add_u32 v162, v3, 10, v1
	v_ashrrev_i32_e32 v1, 31, v0
	v_lshrrev_b32_e32 v1, 22, v1
	v_add_u32_e32 v1, v0, v1
	v_ashrrev_i32_e32 v8, 10, v1
	v_mul_i32_i24_e32 v1, 0x400, v8
	v_sub_u32_e32 v0, v0, v1
	v_lshrrev_b32_e32 v1, 4, v0
	v_bitop3_b32 v0, v1, v0, 32 bitop3:0x6c
	v_ashrrev_i32_e32 v1, 31, v0
	v_lshrrev_b32_e32 v1, 26, v1
	v_add_u32_e32 v1, v0, v1
	v_lshlrev_b32_e32 v3, 3, v8
	v_ashrrev_i32_e32 v9, 6, v1
	v_and_b32_e32 v3, -16, v3
	v_add_u32_e32 v3, v9, v3
	v_and_b32_e32 v10, 3, v9
	s_ashr_i32 s36, s88, 31
	v_and_or_b32 v10, v3, s0, v10
	s_lshr_b32 s0, s36, 29
	s_add_i32 s0, s88, s0
	s_ashr_i32 s2, s0, 3
	s_and_b32 s0, s0, -8
	s_lshr_b32 s1, s89, 8
	s_sub_i32 s0, s88, s0
	s_cmp_lt_i32 s0, 0
	s_movk_i32 s37, 0xa1
	s_cselect_b32 s3, s37, 0xa0
	s_mul_i32 s0, s3, s0
	s_add_i32 s0, s0, s2
	s_mul_hi_i32 s2, s0, 0x66666667
	s_lshr_b32 s3, s2, 31
	s_ashr_i32 s2, s2, 9
	s_add_i32 s2, s2, s3
	s_mulk_i32 s2, 0x500
	s_sub_i32 s0, s0, s2
	s_sext_i32_i16 s2, s0
	s_mulk_i32 s2, 0x6667
	s_lshr_b32 s3, s2, 31
	s_ashr_i32 s2, s2, 22
	s_add_i32 s2, s2, s3
	s_lshl_b32 s3, s2, 3
	s_mulk_i32 s2, 0xa0
	s_sub_i32 s2, s0, s2
	s_sext_i32_i16 s0, s2
	s_bfe_u32 s0, s0, 0x3001c
	s_add_i32 s4, s2, s0
	s_sext_i32_i16 s0, s4
	s_and_b32 s4, s4, 0xfff8
	s_sub_i32 s2, s2, s4
	s_sext_i32_i16 s2, s2
	v_lshrrev_b32_e32 v11, 2, v3
	v_lshlrev_b32_e32 v12, 1, v3
	v_and_b32_e32 v1, 0xc0, v1
	s_lshr_b32 s0, s0, 3
	s_add_i32 s2, s3, s2
	v_and_b32_e32 v11, 4, v11
	v_and_b32_e32 v12, 24, v12
	v_sub_u32_e32 v0, v0, v1
	s_ashr_i32 s3, s2, 31
	s_bfe_i64 s[4:5], s[0:1], 0x100000
	v_or3_b32 v11, v10, v11, v12
	v_lshlrev_b32_e32 v10, 5, v8
	v_ashrrev_i16_sdwa v0, v2, sext(v0) dst_sel:DWORD dst_unused:UNUSED_PAD src0_sel:DWORD src1_sel:BYTE_0
	s_lshl_b64 s[4:5], s[4:5], 18
	s_lshl_b64 s[6:7], s[2:3], 18
	v_and_b32_e32 v12, 32, v10
	v_bfe_i32 v10, v0, 0, 16
	s_add_u32 s24, s31, s4
	v_add_lshl_u32 v0, v12, v10, 1
	s_addc_u32 s25, s34, s5
	s_add_i32 s38, s35, 0
	v_lshl_add_u32 v164, v11, 7, v0
	s_add_i32 m0, s38, 0x10000
	v_lshl_add_u32 v166, v3, 10, v0
	global_load_lds_dwordx4 v164, s[24:25]
	s_add_i32 m0, s38, 0x12000
	s_add_u32 s4, s24, 0x4000
	global_load_lds_dwordx4 v160, s[24:25]
	s_addc_u32 s5, s25, 0
	s_add_i32 m0, s38, 0x14000
	v_mov_b32_e32 v169, 0
	global_load_lds_dwordx4 v164, s[4:5]
	s_add_i32 m0, s38, 0x16000
	s_add_u32 s26, s11, s6
	s_addc_u32 s27, s30, s7
	s_add_i32 s39, s38, 0x2000
	global_load_lds_dwordx4 v160, s[4:5]
	s_mov_b32 m0, s38
	s_add_u32 s4, s26, 0x20000
	global_load_lds_dwordx4 v166, s[26:27]
	s_mov_b32 m0, s39
	s_addc_u32 s5, s27, 0
	s_add_i32 s40, s38, 0x4000
	global_load_lds_dwordx4 v162, s[26:27]
	s_mov_b32 m0, s40
	s_add_i32 s41, s38, 0x6000
	global_load_lds_dwordx4 v166, s[4:5]
	s_mov_b32 m0, s41
	v_mov_b32_e32 v167, v169
	global_load_lds_dwordx4 v162, s[4:5]
	v_mov_b32_e32 v163, v169
	s_cmp_eq_u32 s1, 1
	s_mov_b32 s3, 0
	v_mov_b32_e32 v165, v169
	v_mov_b32_e32 v161, v169
	v_lshl_add_u64 v[0:1], s[26:27], 0, v[166:167]
	s_cselect_b64 s[4:5], -1, 0
	s_cmp_lg_u32 s1, 1
	v_lshl_add_u64 v[2:3], s[26:27], 0, v[162:163]
	s_cbranch_scc1 .LBB0_2947
	s_barrier

.LBB0_2960:
	v_readlane_b32 s6, v253, 23
	v_readlane_b32 s7, v253, 24
	s_mov_b32 s88, s98
	s_setprio 0
	s_cmp_lt_u32 s7, 52
	s_cbranch_scc1 .LBB0_3010
	v_readlane_b32 s0, v253, 20
	s_waitcnt vmcnt(0)
	s_lshl_b32 s0, s0, 6
	s_sub_i32 s0, 0, s0
	s_waitcnt vmcnt(0)
	s_barrier
	v_mbcnt_lo_u32_b32 v0, -1, 0
	v_mbcnt_hi_u32_b32 v0, -1, v0
	s_nop 0
	v_cmp_eq_u32_e32 vcc, s0, v0
	s_and_saveexec_b64 s[0:1], vcc
	s_cbranch_execz .LBB0_3009
	s_add_i32 s2, 0, 0x20160
	v_mov_b32_e32 v0, s2
	s_waitcnt vmcnt(0) expcnt(0) lgkmcnt(0)
	ds_read_b32 v2, v0
	s_add_i32 s2, 0, 0x20164
	v_mov_b32_e32 v0, s2
	ds_read_b32 v0, v0
	s_waitcnt lgkmcnt(1)
	v_cmp_ne_u32_e32 vcc, 0, v2
	s_cbranch_vccnz .LBB0_2977
	v_readlane_b32 s2, v253, 0
	v_readlane_b32 s3, v253, 1
	s_load_dwordx2 s[6:7], s[2:3], 0x4
	s_add_u32 s2, s94, 0x4200
	s_addc_u32 s3, s95, 0
	s_add_u32 s4, s94, 0x4400
	s_addc_u32 s5, s95, 0
	s_waitcnt lgkmcnt(0)
	s_mul_i32 s33, s6, s90
	s_add_u32 s6, s94, 0x4500
	s_mul_i32 s33, s33, s7
	s_addc_u32 s7, s95, 0
	s_add_u32 s8, s94, 0x4600
	s_addc_u32 s9, s95, 0
	s_add_u32 s10, s94, 0x4700
	s_addc_u32 s11, s95, 0
	s_add_u32 s12, s94, 0x4800
	s_addc_u32 s13, s95, 0
	s_add_u32 s14, s94, 0x4900
	s_addc_u32 s15, s95, 0
	s_add_u32 s16, s94, 0x4a00
	s_addc_u32 s17, s95, 0
	s_add_u32 s18, s94, 0x4b00
	s_addc_u32 s19, s95, 0
	s_add_u32 s20, s94, 0x4c00
	s_addc_u32 s21, s95, 0
	s_add_u32 s22, s94, 0x4d00
	s_addc_u32 s23, s95, 0
	s_add_u32 s24, s94, 0x4e00
	s_addc_u32 s25, s95, 0
	s_add_u32 s26, s94, 0x4f00
	s_addc_u32 s27, s95, 0
	s_add_u32 s28, s94, 0x5000
	s_addc_u32 s29, s95, 0
	s_add_u32 s30, s94, 0x5100
	s_addc_u32 s31, s95, 0
	s_add_u32 s34, s94, 0x5200
	s_addc_u32 s35, s95, 0
	s_add_u32 s36, s94, 0x5300
	s_addc_u32 s37, s95, 0
	s_mov_b32 s44, 1
	v_mov_b32_e32 v16, 0
	s_branch .LBB0_2965

.LBB0_3225:
	s_cmp_gt_i32 s6, 54
	s_cselect_b64 s[0:1], -1, 0
	s_cmp_lt_i32 s7, 55
	s_cselect_b64 s[2:3], -1, 0
	s_or_b64 s[0:1], s[0:1], s[2:3]
	s_and_b64 vcc, exec, s[0:1]
	s_cbranch_vccnz .LBB0_3300
	s_mov_b32 s98, s88
	s_and_b32 s99, s88, 31
	s_lshl_b32 s99, s99, 3
	s_lshr_b32 s88, s88, 5
	s_or_b32 s88, s88, s99
	v_readlane_b32 s99, v253, 20
	s_nop 3
	s_cmp_lt_u32 s99, 4
	s_cbranch_scc1 .Lgprio_16
	s_setprio 1

.LBB0_3250:
	v_readlane_b32 s6, v253, 23
	v_readlane_b32 s7, v253, 24
	s_mov_b32 s88, s98
	s_setprio 0
	s_cmp_lt_u32 s7, 56
	s_cbranch_scc1 .LBB0_3300
	v_readlane_b32 s0, v253, 20
	s_waitcnt vmcnt(0)
	s_lshl_b32 s0, s0, 6
	s_sub_i32 s0, 0, s0
	s_waitcnt vmcnt(0)
	s_barrier
	v_mbcnt_lo_u32_b32 v0, -1, 0
	v_mbcnt_hi_u32_b32 v0, -1, v0
	s_nop 0
	v_cmp_eq_u32_e32 vcc, s0, v0
	s_and_saveexec_b64 s[0:1], vcc
	s_cbranch_execz .LBB0_3299
	s_add_i32 s2, 0, 0x20160
	v_mov_b32_e32 v0, s2
	s_waitcnt vmcnt(0) expcnt(0) lgkmcnt(0)
	ds_read_b32 v2, v0
	s_add_i32 s2, 0, 0x20164
	v_mov_b32_e32 v0, s2
	ds_read_b32 v0, v0
	s_waitcnt lgkmcnt(1)
	v_cmp_ne_u32_e32 vcc, 0, v2
	s_cbranch_vccnz .LBB0_3267
	v_readlane_b32 s2, v253, 0
	v_readlane_b32 s3, v253, 1
	s_load_dwordx2 s[6:7], s[2:3], 0x4
	s_add_u32 s2, s94, 0x4200
	s_addc_u32 s3, s95, 0
	s_add_u32 s4, s94, 0x4400
	s_addc_u32 s5, s95, 0
	s_waitcnt lgkmcnt(0)
	s_mul_i32 s33, s6, s90
	s_add_u32 s6, s94, 0x4500
	s_mul_i32 s33, s33, s7
	s_addc_u32 s7, s95, 0
	s_add_u32 s8, s94, 0x4600
	s_addc_u32 s9, s95, 0
	s_add_u32 s10, s94, 0x4700
	s_addc_u32 s11, s95, 0
	s_add_u32 s12, s94, 0x4800
	s_addc_u32 s13, s95, 0
	s_add_u32 s14, s94, 0x4900
	s_addc_u32 s15, s95, 0
	s_add_u32 s16, s94, 0x4a00
	s_addc_u32 s17, s95, 0
	s_add_u32 s18, s94, 0x4b00
	s_addc_u32 s19, s95, 0
	s_add_u32 s20, s94, 0x4c00
	s_addc_u32 s21, s95, 0
	s_add_u32 s22, s94, 0x4d00
	s_addc_u32 s23, s95, 0
	s_add_u32 s24, s94, 0x4e00
	s_addc_u32 s25, s95, 0
	s_add_u32 s26, s94, 0x4f00
	s_addc_u32 s27, s95, 0
	s_add_u32 s28, s94, 0x5000
	s_addc_u32 s29, s95, 0
	s_add_u32 s30, s94, 0x5100
	s_addc_u32 s31, s95, 0
	s_add_u32 s34, s94, 0x5200
	s_addc_u32 s35, s95, 0
	s_add_u32 s36, s94, 0x5300
	s_addc_u32 s37, s95, 0
	s_mov_b32 s44, 1
	v_mov_b32_e32 v16, 0
	s_branch .LBB0_3255

.LBB0_3598:
	s_cmp_gt_i32 s6, 57
	s_cselect_b64 s[0:1], -1, 0
	s_cmp_lt_i32 s7, 58
	s_cselect_b64 s[2:3], -1, 0
	s_or_b64 s[0:1], s[0:1], s[2:3]
	s_and_b64 vcc, exec, s[0:1]
	s_cbranch_vccnz .LBB0_3713
	s_mov_b32 s98, s88
	s_and_b32 s99, s88, 31
	s_lshl_b32 s99, s99, 3
	s_lshr_b32 s88, s88, 5
	s_or_b32 s88, s88, s99
	v_readlane_b32 s99, v253, 20
	s_nop 3
	s_cmp_lt_u32 s99, 4
	s_cbranch_scc1 .Lgprio_17
	s_setprio 1
.Lgprio_17:
	s_waitcnt vmcnt(0)
	v_mov_b32_e32 v1, 0x420000
	v_mbcnt_lo_u32_b32 v0, -1, 0
	v_mbcnt_hi_u32_b32 v0, -1, v0
	global_load_dword v1, v1, s[94:95]
	s_and_b32 s0, s89, 0xffffffc0
	s_movk_i32 s1, 0x140
	v_add_u32_e32 v0, s0, v0
	s_add_u32 s2, s94, 0x420000
	s_addc_u32 s3, s95, 0
	v_cmp_gt_i32_e32 vcc, s1, v0
	s_waitcnt vmcnt(0)
	v_readfirstlane_b32 s17, v1
	s_and_saveexec_b64 s[0:1], vcc
	s_cbranch_execz .LBB0_3601
	v_ashrrev_i32_e32 v1, 31, v0
	v_lshl_add_u64 v[2:3], v[0:1], 2, s[2:3]
	global_load_dword v1, v[2:3], off offset:4
	v_lshl_add_u32 v2, v0, 2, 0
	v_add_u32_e32 v2, 0x22400, v2
	s_waitcnt vmcnt(0)
	ds_write_b32 v2, v1

.LBB0_3663:
	v_readlane_b32 s6, v253, 23
	v_readlane_b32 s7, v253, 24
	s_mov_b32 s88, s98
	s_setprio 0
	s_cmp_lt_u32 s7, 59
	s_cbranch_scc1 .LBB0_3713
	v_readlane_b32 s0, v253, 20
	s_waitcnt vmcnt(0)
	s_lshl_b32 s0, s0, 6
	s_sub_i32 s0, 0, s0
	s_waitcnt vmcnt(0)
	s_barrier
	v_mbcnt_lo_u32_b32 v0, -1, 0
	v_mbcnt_hi_u32_b32 v0, -1, v0
	s_nop 0
	v_cmp_eq_u32_e32 vcc, s0, v0
	s_and_saveexec_b64 s[0:1], vcc
	s_cbranch_execz .LBB0_3712
	s_add_i32 s2, 0, 0x20160
	v_mov_b32_e32 v0, s2
	s_waitcnt vmcnt(0) expcnt(0) lgkmcnt(0)
	ds_read_b32 v2, v0
	s_add_i32 s2, 0, 0x20164
	v_mov_b32_e32 v0, s2
	ds_read_b32 v0, v0
	s_waitcnt lgkmcnt(1)
	v_cmp_ne_u32_e32 vcc, 0, v2
	s_cbranch_vccnz .LBB0_3680
	v_readlane_b32 s2, v253, 0
	v_readlane_b32 s3, v253, 1
	s_load_dwordx2 s[6:7], s[2:3], 0x4
	s_add_u32 s2, s94, 0x4200
	s_addc_u32 s3, s95, 0
	s_add_u32 s4, s94, 0x4400
	s_addc_u32 s5, s95, 0
	s_waitcnt lgkmcnt(0)
	s_mul_i32 s33, s6, s90
	s_add_u32 s6, s94, 0x4500
	s_mul_i32 s33, s33, s7
	s_addc_u32 s7, s95, 0
	s_add_u32 s8, s94, 0x4600
	s_addc_u32 s9, s95, 0
	s_add_u32 s10, s94, 0x4700
	s_addc_u32 s11, s95, 0
	s_add_u32 s12, s94, 0x4800
	s_addc_u32 s13, s95, 0
	s_add_u32 s14, s94, 0x4900
	s_addc_u32 s15, s95, 0
	s_add_u32 s16, s94, 0x4a00
	s_addc_u32 s17, s95, 0
	s_add_u32 s18, s94, 0x4b00
	s_addc_u32 s19, s95, 0
	s_add_u32 s20, s94, 0x4c00
	s_addc_u32 s21, s95, 0
	s_add_u32 s22, s94, 0x4d00
	s_addc_u32 s23, s95, 0
	s_add_u32 s24, s94, 0x4e00
	s_addc_u32 s25, s95, 0
	s_add_u32 s26, s94, 0x4f00
	s_addc_u32 s27, s95, 0
	s_add_u32 s28, s94, 0x5000
	s_addc_u32 s29, s95, 0
	s_add_u32 s30, s94, 0x5100
	s_addc_u32 s31, s95, 0
	s_add_u32 s34, s94, 0x5200
	s_addc_u32 s35, s95, 0
	s_add_u32 s36, s94, 0x5300
	s_addc_u32 s37, s95, 0
	s_mov_b32 s44, 1
	v_mov_b32_e32 v16, 0
	s_branch .LBB0_3668

.LBB0_3713:
	s_cmp_gt_i32 s6, 58
	s_cselect_b64 s[0:1], -1, 0
	s_cmp_lt_i32 s7, 59
	s_cselect_b64 s[2:3], -1, 0
	s_or_b64 s[0:1], s[0:1], s[2:3]
	s_and_b64 vcc, exec, s[0:1]
	s_cbranch_vccnz .LBB0_3792
	s_mov_b32 s98, s88
	s_and_b32 s99, s88, 31
	s_lshl_b32 s99, s99, 3
	s_lshr_b32 s88, s88, 5
	s_or_b32 s88, s88, s99
	v_readlane_b32 s99, v253, 20
	s_nop 3
	s_cmp_lt_u32 s99, 4
	s_cbranch_scc1 .Lgprio_18
	s_setprio 1
.Lgprio_18:
	s_waitcnt vmcnt(0)
	v_mov_b32_e32 v1, 0x420000
	v_mbcnt_lo_u32_b32 v0, -1, 0
	v_mbcnt_hi_u32_b32 v0, -1, v0
	global_load_dword v1, v1, s[94:95]
	s_and_b32 s0, s89, 0xffffffc0
	s_movk_i32 s1, 0x140
	v_add_u32_e32 v0, s0, v0
	s_add_u32 s2, s94, 0x420000
	s_addc_u32 s3, s95, 0
	v_cmp_gt_i32_e32 vcc, s1, v0
	s_waitcnt vmcnt(0)
	v_readfirstlane_b32 s9, v1
	s_and_saveexec_b64 s[0:1], vcc
	s_cbranch_execz .LBB0_3716
	v_ashrrev_i32_e32 v1, 31, v0
	v_lshl_add_u64 v[2:3], v[0:1], 2, s[2:3]
	global_load_dword v1, v[2:3], off offset:4
	v_lshl_add_u32 v0, v0, 2, 0
	v_add_u32_e32 v0, 0x22400, v0
	s_waitcnt vmcnt(0)
	ds_write_b32 v0, v1

.LBB0_3742:
	v_readlane_b32 s6, v253, 23
	v_readlane_b32 s7, v253, 24
	s_mov_b32 s88, s98
	s_setprio 0
	s_cmp_lt_u32 s7, 60
	s_cbranch_scc1 .LBB0_3792
	v_readlane_b32 s0, v253, 20
	s_waitcnt vmcnt(0)
	s_lshl_b32 s0, s0, 6
	s_sub_i32 s0, 0, s0
	s_waitcnt vmcnt(0)
	s_barrier
	v_mbcnt_lo_u32_b32 v0, -1, 0
	v_mbcnt_hi_u32_b32 v0, -1, v0
	s_nop 0
	v_cmp_eq_u32_e32 vcc, s0, v0
	s_and_saveexec_b64 s[0:1], vcc
	s_cbranch_execz .LBB0_3791
	s_add_i32 s2, 0, 0x20160
	v_mov_b32_e32 v0, s2
	s_waitcnt vmcnt(0) expcnt(0) lgkmcnt(0)
	ds_read_b32 v2, v0
	s_add_i32 s2, 0, 0x20164
	v_mov_b32_e32 v0, s2
	ds_read_b32 v0, v0
	s_waitcnt lgkmcnt(1)
	v_cmp_ne_u32_e32 vcc, 0, v2
	s_cbranch_vccnz .LBB0_3759
	v_readlane_b32 s2, v253, 0
	v_readlane_b32 s3, v253, 1
	s_load_dwordx2 s[6:7], s[2:3], 0x4
	s_add_u32 s2, s94, 0x4200
	s_addc_u32 s3, s95, 0
	s_add_u32 s4, s94, 0x4400
	s_addc_u32 s5, s95, 0
	s_waitcnt lgkmcnt(0)
	s_mul_i32 s33, s6, s90
	s_add_u32 s6, s94, 0x4500
	s_mul_i32 s33, s33, s7
	s_addc_u32 s7, s95, 0
	s_add_u32 s8, s94, 0x4600
	s_addc_u32 s9, s95, 0
	s_add_u32 s10, s94, 0x4700
	s_addc_u32 s11, s95, 0
	s_add_u32 s12, s94, 0x4800
	s_addc_u32 s13, s95, 0
	s_add_u32 s14, s94, 0x4900
	s_addc_u32 s15, s95, 0
	s_add_u32 s16, s94, 0x4a00
	s_addc_u32 s17, s95, 0
	s_add_u32 s18, s94, 0x4b00
	s_addc_u32 s19, s95, 0
	s_add_u32 s20, s94, 0x4c00
	s_addc_u32 s21, s95, 0
	s_add_u32 s22, s94, 0x4d00
	s_addc_u32 s23, s95, 0
	s_add_u32 s24, s94, 0x4e00
	s_addc_u32 s25, s95, 0
	s_add_u32 s26, s94, 0x4f00
	s_addc_u32 s27, s95, 0
	s_add_u32 s28, s94, 0x5000
	s_addc_u32 s29, s95, 0
	s_add_u32 s30, s94, 0x5100
	s_addc_u32 s31, s95, 0
	s_add_u32 s34, s94, 0x5200
	s_addc_u32 s35, s95, 0
	s_add_u32 s36, s94, 0x5300
	s_addc_u32 s37, s95, 0
	s_mov_b32 s44, 1
	v_mov_b32_e32 v16, 0
	s_branch .LBB0_3747
